# stack2_sc1
# speedup vs baseline: 1.0043x; 1.0043x over previous
.LBB2_2:
	s_or_b64 exec, exec, s[12:13]
	v_lshrrev_b32_e32 v68, 7, v0
	s_lshl_b32 s0, s2, 4
	v_lshl_or_b32 v34, v68, 2, s0
	v_lshrrev_b32_e32 v2, 1, v0
	v_ashrrev_i32_e32 v35, 31, v34
	v_and_b32_e32 v69, 32, v2
	v_lshlrev_b64 v[2:3], 8, v[34:35]
	v_lshl_add_u64 v[2:3], s[4:5], 0, v[2:3]
	v_lshlrev_b32_e32 v66, 2, v69
	v_lshl_add_u64 v[2:3], v[2:3], 0, v[66:67]
	v_lshlrev_b32_e32 v36, 2, v1
	v_mov_b32_e32 v37, v67
	v_lshl_add_u64 v[2:3], v[2:3], 0, v[36:37]
	v_lshlrev_b32_e32 v38, 22, v72
	v_mov_b32_e32 v39, v67
	v_lshl_add_u64 v[4:5], v[2:3], 0, v[38:39]
	v_or_b32_e32 v40, 0x800000, v38
	v_mov_b32_e32 v41, v67
	global_load_dword v6, v[4:5], off
	v_lshl_add_u64 v[4:5], v[2:3], 0, v[40:41]
	v_or_b32_e32 v42, 0x1000000, v38
	v_mov_b32_e32 v43, v67
	global_load_dword v18, v[4:5], off
	v_lshl_add_u64 v[4:5], v[2:3], 0, v[42:43]
	v_or_b32_e32 v44, 0x1800000, v38
	v_mov_b32_e32 v45, v67
	global_load_dword v19, v[4:5], off
	v_lshl_add_u64 v[4:5], v[2:3], 0, v[44:45]
	v_or_b32_e32 v46, 0x2000000, v38
	v_mov_b32_e32 v47, v67
	global_load_dword v20, v[4:5], off
	v_lshl_add_u64 v[4:5], v[2:3], 0, v[46:47]
	v_or_b32_e32 v48, 0x2800000, v38
	v_mov_b32_e32 v49, v67
	global_load_dword v21, v[4:5], off
	v_lshl_add_u64 v[4:5], v[2:3], 0, v[48:49]
	v_or_b32_e32 v50, 0x3000000, v38
	v_mov_b32_e32 v51, v67
	global_load_dword v22, v[4:5], off
	v_lshl_add_u64 v[4:5], v[2:3], 0, v[50:51]
	v_or_b32_e32 v52, 0x3800000, v38
	v_mov_b32_e32 v53, v67
	global_load_dword v23, v[4:5], off
	v_lshl_add_u64 v[4:5], v[2:3], 0, v[52:53]
	v_or_b32_e32 v54, 0x4000000, v38
	v_mov_b32_e32 v55, v67
	global_load_dword v24, v[4:5], off
	v_lshl_add_u64 v[4:5], v[2:3], 0, v[54:55]
	v_or_b32_e32 v56, 0x4800000, v38
	v_mov_b32_e32 v57, v67
	global_load_dword v25, v[4:5], off
	v_lshl_add_u64 v[4:5], v[2:3], 0, v[56:57]
	v_or_b32_e32 v58, 0x5000000, v38
	v_mov_b32_e32 v59, v67
	global_load_dword v26, v[4:5], off
	v_lshl_add_u64 v[4:5], v[2:3], 0, v[58:59]
	v_or_b32_e32 v60, 0x5800000, v38
	v_mov_b32_e32 v61, v67
	s_mov_b64 s[6:7], 0x6000000
	global_load_dword v27, v[4:5], off
	v_lshl_add_u64 v[4:5], v[2:3], 0, v[60:61]
	v_lshl_add_u64 v[2:3], v[2:3], 0, s[6:7]
	global_load_dword v28, v[4:5], off
	global_load_dword v29, v[2:3], off
	v_or_b32_e32 v2, 1, v34
	v_ashrrev_i32_e32 v3, 31, v2
	v_lshlrev_b64 v[2:3], 8, v[2:3]
	v_lshl_add_u64 v[2:3], s[4:5], 0, v[2:3]
	v_lshl_add_u64 v[2:3], v[2:3], 0, v[66:67]
	v_lshl_add_u64 v[2:3], v[2:3], 0, v[36:37]
	v_lshl_add_u64 v[4:5], v[2:3], 0, v[38:39]
	global_load_dword v30, v[4:5], off
	v_lshl_add_u64 v[4:5], v[2:3], 0, v[40:41]
	global_load_dword v35, v[4:5], off
	v_lshl_add_u64 v[4:5], v[2:3], 0, v[42:43]
	global_load_dword v63, v[4:5], off
	v_lshl_add_u64 v[4:5], v[2:3], 0, v[44:45]
	global_load_dword v64, v[4:5], off
	v_lshl_add_u64 v[4:5], v[2:3], 0, v[46:47]
	global_load_dword v65, v[4:5], off
	v_lshl_add_u64 v[4:5], v[2:3], 0, v[48:49]
	global_load_dword v83, v[4:5], off
	v_lshl_add_u64 v[4:5], v[2:3], 0, v[50:51]
	global_load_dword v84, v[4:5], off
	v_lshl_add_u64 v[4:5], v[2:3], 0, v[52:53]
	global_load_dword v85, v[4:5], off
	v_lshl_add_u64 v[4:5], v[2:3], 0, v[54:55]
	global_load_dword v86, v[4:5], off
	v_lshl_add_u64 v[4:5], v[2:3], 0, v[56:57]
	global_load_dword v87, v[4:5], off
	v_lshl_add_u64 v[4:5], v[2:3], 0, v[58:59]
	global_load_dword v88, v[4:5], off
	v_lshl_add_u64 v[4:5], v[2:3], 0, v[60:61]
	global_load_dword v89, v[4:5], off
	v_lshl_add_u64 v[2:3], v[2:3], 0, s[6:7]
	global_load_dword v90, v[2:3], off
	s_waitcnt vmcnt(13)
	s_mov_b32 s0, 0xff61b1e6
	v_mfma_f32_32x32x2_f32 v[2:17], v62, v6, 0
	v_or_b32_e32 v1, v69, v1
	v_lshlrev_b32_e32 v1, 9, v1
	v_mfma_f32_32x32x2_f32 v[2:17], v82, v18, v[2:17]
	v_or_b32_e32 v18, 2, v34
	v_or_b32_e32 v34, 3, v34
	v_mfma_f32_32x32x2_f32 v[2:17], v81, v19, v[2:17]
	v_ashrrev_i32_e32 v19, 31, v18
	v_lshlrev_b64 v[18:19], 8, v[18:19]
	v_lshl_add_u64 v[18:19], s[4:5], 0, v[18:19]
	v_lshl_add_u64 v[18:19], v[18:19], 0, v[66:67]
	v_lshl_add_u64 v[18:19], v[18:19], 0, v[36:37]
	v_mfma_f32_32x32x2_f32 v[2:17], v80, v20, v[2:17]
	v_mfma_f32_32x32x2_f32 v[2:17], v79, v21, v[2:17]
	v_lshl_add_u64 v[20:21], v[18:19], 0, v[38:39]
	global_load_dword v91, v[20:21], off
	v_lshl_add_u64 v[20:21], v[18:19], 0, v[40:41]
	global_load_dword v92, v[20:21], off
	v_lshl_add_u64 v[20:21], v[18:19], 0, v[42:43]
	global_load_dword v93, v[20:21], off
	v_lshl_add_u64 v[20:21], v[18:19], 0, v[44:45]
	global_load_dword v94, v[20:21], off
	v_lshl_add_u64 v[20:21], v[18:19], 0, v[46:47]
	global_load_dword v95, v[20:21], off
	v_lshl_add_u64 v[20:21], v[18:19], 0, v[48:49]
	global_load_dword v96, v[20:21], off
	v_lshl_add_u64 v[20:21], v[18:19], 0, v[50:51]
	global_load_dword v97, v[20:21], off
	v_lshl_add_u64 v[20:21], v[18:19], 0, v[52:53]
	v_mfma_f32_32x32x2_f32 v[2:17], v78, v22, v[2:17]
	global_load_dword v98, v[20:21], off
	v_lshl_add_u64 v[20:21], v[18:19], 0, v[54:55]
	global_load_dword v99, v[20:21], off
	v_lshl_add_u64 v[20:21], v[18:19], 0, v[56:57]
	global_load_dword v100, v[20:21], off
	v_lshl_add_u64 v[20:21], v[18:19], 0, v[58:59]
	global_load_dword v101, v[20:21], off
	v_lshl_add_u64 v[20:21], v[18:19], 0, v[60:61]
	global_load_dword v102, v[20:21], off
	v_lshl_add_u64 v[18:19], v[18:19], 0, s[6:7]
	global_load_dword v103, v[18:19], off
	s_waitcnt vmcnt(13)
	v_mfma_f32_32x32x2_f32 v[2:17], v77, v23, v[2:17]
	v_mfma_f32_32x32x2_f32 v[2:17], v76, v24, v[2:17]
	v_mfma_f32_32x32x2_f32 v[2:17], v75, v25, v[2:17]
	v_mfma_f32_32x32x2_f32 v[2:17], v74, v26, v[2:17]
	v_mfma_f32_32x32x2_f32 v[2:17], v73, v27, v[2:17]
	v_mfma_f32_32x32x2_f32 v[2:17], v71, v28, v[2:17]
	v_mfma_f32_32x32x2_f32 v[2:17], v70, v29, v[2:17]
	v_mfma_f32_32x32x2_f32 v[18:33], v62, v30, 0
	v_mfma_f32_32x32x2_f32 v[18:33], v82, v35, v[18:33]
	v_ashrrev_i32_e32 v35, 31, v34
	v_lshlrev_b64 v[34:35], 8, v[34:35]
	v_lshl_add_u64 v[34:35], s[4:5], 0, v[34:35]
	v_lshl_add_u64 v[34:35], v[34:35], 0, v[66:67]
	v_lshl_add_u64 v[34:35], v[34:35], 0, v[36:37]
	v_lshl_add_u64 v[36:37], v[34:35], 0, v[38:39]
	v_mfma_f32_32x32x2_f32 v[18:33], v81, v63, v[18:33]
	global_load_dword v63, v[36:37], off
	v_lshl_add_u64 v[36:37], v[34:35], 0, v[40:41]
	global_load_dword v66, v[36:37], off
	v_lshl_add_u64 v[36:37], v[34:35], 0, v[42:43]
	v_mfma_f32_32x32x2_f32 v[18:33], v80, v64, v[18:33]
	v_mfma_f32_32x32x2_f32 v[18:33], v79, v65, v[18:33]
	v_mfma_f32_32x32x2_f32 v[18:33], v78, v83, v[18:33]
	global_load_dword v83, v[36:37], off
	v_lshl_add_u64 v[36:37], v[34:35], 0, v[44:45]
	v_mfma_f32_32x32x2_f32 v[18:33], v77, v84, v[18:33]
	global_load_dword v84, v[36:37], off
	v_lshl_add_u64 v[36:37], v[34:35], 0, v[46:47]
	v_mfma_f32_32x32x2_f32 v[18:33], v76, v85, v[18:33]
	global_load_dword v85, v[36:37], off
	v_lshl_add_u64 v[36:37], v[34:35], 0, v[48:49]
	v_mfma_f32_32x32x2_f32 v[18:33], v75, v86, v[18:33]
	global_load_dword v86, v[36:37], off
	v_lshl_add_u64 v[36:37], v[34:35], 0, v[50:51]
	v_mfma_f32_32x32x2_f32 v[18:33], v74, v87, v[18:33]
	global_load_dword v87, v[36:37], off
	v_lshl_add_u64 v[36:37], v[34:35], 0, v[52:53]
	v_mfma_f32_32x32x2_f32 v[18:33], v73, v88, v[18:33]
	global_load_dword v88, v[36:37], off
	v_lshl_add_u64 v[36:37], v[34:35], 0, v[54:55]
	v_mfma_f32_32x32x2_f32 v[18:33], v71, v89, v[18:33]
	global_load_dword v89, v[36:37], off
	v_lshl_add_u64 v[36:37], v[34:35], 0, v[56:57]
	v_mfma_f32_32x32x2_f32 v[18:33], v70, v90, v[18:33]
	global_load_dword v90, v[36:37], off
	v_lshl_add_u64 v[36:37], v[34:35], 0, v[58:59]
	global_load_dword v104, v[36:37], off
	v_lshl_add_u64 v[36:37], v[34:35], 0, v[60:61]
	global_load_dword v105, v[36:37], off
	v_lshl_add_u64 v[34:35], v[34:35], 0, s[6:7]
	global_load_dword v106, v[34:35], off
	s_waitcnt vmcnt(13)
	s_nop 14
	v_max3_f32 v2, v2, s0, v18
	s_waitcnt vmcnt(0)
	v_mfma_f32_32x32x2_f32 v[34:49], v62, v91, 0
	v_max3_f32 v3, v3, s0, v19
	v_max3_f32 v4, v4, s0, v20
	v_max3_f32 v5, v5, s0, v21
	v_max3_f32 v6, v6, s0, v22
	v_max3_f32 v7, v7, s0, v23
	v_max3_f32 v8, v8, s0, v24
	v_max3_f32 v9, v9, s0, v25
	v_lshlrev_b32_e32 v18, 5, v68
	v_max3_f32 v10, v10, s0, v26
	v_max3_f32 v11, v11, s0, v27
	v_max3_f32 v12, v12, s0, v28
	v_max3_f32 v13, v13, s0, v29
	v_max3_f32 v14, v14, s0, v30
	v_max3_f32 v15, v15, s0, v31
	v_max3_f32 v16, v16, s0, v32
	v_mfma_f32_32x32x2_f32 v[50:65], v62, v63, 0
	v_max3_f32 v17, v17, s0, v33
	s_lshl_b32 s0, s2, 2
	s_mov_b32 s2, 0x7f000
	v_mfma_f32_32x32x2_f32 v[34:49], v82, v92, v[34:49]
	v_mfma_f32_32x32x2_f32 v[50:65], v82, v66, v[50:65]
	v_lshlrev_b32_e32 v66, 4, v72
	v_or3_b32 v1, v1, v18, v66
	v_mfma_f32_32x32x2_f32 v[34:49], v81, v93, v[34:49]
	v_mfma_f32_32x32x2_f32 v[50:65], v81, v83, v[50:65]
	v_mfma_f32_32x32x2_f32 v[34:49], v80, v94, v[34:49]
	v_mfma_f32_32x32x2_f32 v[50:65], v80, v84, v[50:65]
	v_mfma_f32_32x32x2_f32 v[34:49], v79, v95, v[34:49]
	v_mfma_f32_32x32x2_f32 v[50:65], v79, v85, v[50:65]
	v_mfma_f32_32x32x2_f32 v[34:49], v78, v96, v[34:49]
	v_mfma_f32_32x32x2_f32 v[50:65], v78, v86, v[50:65]
	v_mfma_f32_32x32x2_f32 v[34:49], v77, v97, v[34:49]
	v_mfma_f32_32x32x2_f32 v[50:65], v77, v87, v[50:65]
	v_mfma_f32_32x32x2_f32 v[34:49], v76, v98, v[34:49]
	v_mfma_f32_32x32x2_f32 v[50:65], v76, v88, v[50:65]
	v_mfma_f32_32x32x2_f32 v[34:49], v75, v99, v[34:49]
	v_mfma_f32_32x32x2_f32 v[50:65], v75, v89, v[50:65]
	v_mfma_f32_32x32x2_f32 v[34:49], v74, v100, v[34:49]
	v_mfma_f32_32x32x2_f32 v[50:65], v74, v90, v[50:65]
	global_load_dwordx4 v[74:77], v66, s[8:9]
	global_load_dwordx4 v[78:81], v66, s[8:9] offset:32
	global_load_dwordx4 v[82:85], v66, s[8:9] offset:64
	global_load_dwordx4 v[86:89], v66, s[8:9] offset:96
	v_mfma_f32_32x32x2_f32 v[34:49], v73, v101, v[34:49]
	v_mfma_f32_32x32x2_f32 v[50:65], v73, v104, v[50:65]
	v_mfma_f32_32x32x2_f32 v[34:49], v71, v102, v[34:49]
	v_mfma_f32_32x32x2_f32 v[50:65], v71, v105, v[50:65]
	v_mfma_f32_32x32x2_f32 v[34:49], v70, v103, v[34:49]
	v_mfma_f32_32x32x2_f32 v[50:65], v70, v106, v[50:65]
	s_nop 15
	s_nop 1
	v_max3_f32 v2, v2, v34, v50
	v_max3_f32 v3, v3, v35, v51
	v_max3_f32 v4, v4, v36, v52
	v_max3_f32 v5, v5, v37, v53
	s_waitcnt vmcnt(3)
	v_add_f32_e32 v2, v2, v74
	v_add_f32_e32 v3, v3, v75
	v_add_f32_e32 v4, v4, v76
	v_add_f32_e32 v5, v5, v77
	v_max3_f32 v6, v6, v38, v54
	v_max3_f32 v7, v7, v39, v55
	v_max3_f32 v8, v8, v40, v56
	v_max3_f32 v9, v9, v41, v57
	v_max_f32_e32 v2, 0, v2
	v_max_f32_e32 v3, 0, v3
	v_max_f32_e32 v4, 0, v4
	v_max_f32_e32 v5, 0, v5
	ds_write_b128 v1, v[2:5]
	s_waitcnt vmcnt(2)
	v_add_f32_e32 v2, v6, v78
	v_add_f32_e32 v3, v7, v79
	v_add_f32_e32 v4, v8, v80
	v_add_f32_e32 v5, v9, v81
	v_max3_f32 v10, v10, v42, v58
	v_max3_f32 v11, v11, v43, v59
	v_max3_f32 v12, v12, v44, v60
	v_max3_f32 v13, v13, v45, v61
	v_max_f32_e32 v2, 0, v2
	v_max_f32_e32 v3, 0, v3
	v_max_f32_e32 v4, 0, v4
	v_max_f32_e32 v5, 0, v5
	ds_write_b128 v1, v[2:5] offset:128
	s_waitcnt vmcnt(1)
	v_add_f32_e32 v2, v10, v82
	v_add_f32_e32 v3, v11, v83
	v_add_f32_e32 v4, v12, v84
	v_add_f32_e32 v5, v13, v85
	v_max3_f32 v14, v14, v46, v62
	v_max3_f32 v15, v15, v47, v63
	v_max3_f32 v16, v16, v48, v64
	v_max3_f32 v17, v17, v49, v65
	v_max_f32_e32 v2, 0, v2
	v_max_f32_e32 v3, 0, v3
	v_max_f32_e32 v4, 0, v4
	v_max_f32_e32 v5, 0, v5
	ds_write_b128 v1, v[2:5] offset:256
	s_waitcnt vmcnt(0)
	v_add_f32_e32 v2, v14, v86
	v_add_f32_e32 v3, v15, v87
	v_add_f32_e32 v4, v16, v88
	v_add_f32_e32 v5, v17, v89
	v_max_f32_e32 v2, 0, v2
	v_max_f32_e32 v3, 0, v3
	v_max_f32_e32 v4, 0, v4
	v_max_f32_e32 v5, 0, v5
	v_lshlrev_b32_e32 v12, 4, v0
	ds_write_b128 v1, v[2:5] offset:384
	s_waitcnt lgkmcnt(0)
	s_barrier
	v_and_b32_e32 v66, 0x70, v12
	v_lshlrev_b32_e32 v13, 9, v0
	ds_read_b128 v[0:3], v12
	v_lshl_add_u64 v[8:9], s[10:11], 0, v[66:67]
	v_and_b32_e32 v66, 0x3f000, v13
	v_lshl_add_u64 v[4:5], v[66:67], 0, s[0:1]
	v_lshlrev_b64 v[4:5], 5, v[4:5]
	v_lshl_add_u64 v[10:11], v[8:9], 0, v[4:5]
	ds_read_b128 v[4:7], v12 offset:8192
	s_waitcnt lgkmcnt(1)
	global_store_dwordx4 v[10:11], v[0:3], off sc1
	s_nop 1
	v_mov_b32_e32 v0, 0x40000
	v_bitop3_b32 v66, v13, s2, v0 bitop3:0xc8
	v_lshl_add_u64 v[0:1], v[66:67], 0, s[0:1]
	v_lshlrev_b64 v[0:1], 5, v[0:1]
	v_lshl_add_u64 v[0:1], v[8:9], 0, v[0:1]
	s_waitcnt lgkmcnt(0)
	global_store_dwordx4 v[0:1], v[4:7], off sc1
	s_mov_b32 s2, 0xbf000
	v_mov_b32_e32 v0, 0x80000
	v_bitop3_b32 v66, v13, s2, v0 bitop3:0xc8
	ds_read_b128 v[0:3], v12 offset:16384
	v_lshl_add_u64 v[4:5], v[66:67], 0, s[0:1]
	v_lshlrev_b64 v[4:5], 5, v[4:5]
	v_lshl_add_u64 v[10:11], v[8:9], 0, v[4:5]
	ds_read_b128 v[4:7], v12 offset:24576
	s_waitcnt lgkmcnt(1)
	global_store_dwordx4 v[10:11], v[0:3], off sc1
	s_mov_b32 s2, 0xff000
	s_nop 0
	v_mov_b32_e32 v0, 0xc0000
	v_bitop3_b32 v66, v13, s2, v0 bitop3:0xc8
	v_lshl_add_u64 v[0:1], v[66:67], 0, s[0:1]
	v_lshlrev_b64 v[0:1], 5, v[0:1]
	v_lshl_add_u64 v[0:1], v[8:9], 0, v[0:1]
	s_waitcnt lgkmcnt(0)
	global_store_dwordx4 v[0:1], v[4:7], off sc1
	s_endpgm

.LBB5_1:
	s_add_i32 s33, s12, 1
	s_lshl_b32 s42, s12, 15
	s_min_u32 s12, s33, 3
	s_lshl_b32 s12, s12, 8
	s_and_b32 s42, s42, 0x8000
	v_lshl_add_u64 v[52:53], v[96:97], 0, s[12:13]
	v_lshl_add_u64 v[80:81], v[100:101], 0, 16
	v_lshl_add_u64 v[82:83], v[100:101], 0, 32
	v_or_b32_e32 v136, s42, v106
	v_lshl_add_u64 v[54:55], v[52:53], 0, 16
	v_lshl_add_u64 v[56:57], v[52:53], 0, 64
	v_lshl_add_u64 v[58:59], v[52:53], 0, s[4:5]
	v_lshl_add_u64 v[60:61], v[52:53], 0, s[6:7]
	v_lshl_add_u64 v[62:63], v[52:53], 0, s[14:15]
	v_lshl_add_u64 v[64:65], v[52:53], 0, s[16:17]
	v_lshl_add_u64 v[66:67], v[52:53], 0, s[18:19]
	v_lshl_add_u64 v[102:103], v[100:101], 0, 48
	global_load_dwordx4 v[48:51], v[52:53], off
	global_load_dwordx4 v[68:71], v[54:55], off
	global_load_dwordx4 v[72:75], v[56:57], off
	global_load_dwordx4 v[76:79], v[58:59], off
	global_load_dwordx4 v[52:55], v[60:61], off
	global_load_dwordx4 v[56:59], v[62:63], off
	global_load_dwordx4 v[60:63], v[64:65], off
	global_load_dwordx4 v[64:67], v[66:67], off
	global_load_dwordx4 v[92:95], v[100:101], off
	global_load_dwordx4 v[88:91], v[80:81], off
	global_load_dwordx4 v[84:87], v[82:83], off
	global_load_dwordx4 v[80:83], v[102:103], off
	s_waitcnt vmcnt(20)
	ds_read_b128 v[108:111], v136
	ds_read_b128 v[112:115], v136 offset:1024
	ds_read_b128 v[116:119], v136 offset:4096
	ds_read_b128 v[120:123], v136 offset:5120
	v_cvt_pk_bf16_f32 v124, v32, v33
	v_cvt_pk_bf16_f32 v125, v34, v35
	v_cvt_pk_bf16_f32 v126, v16, v17
	v_cvt_pk_bf16_f32 v127, v18, v19
	s_min_i32 s12, s1, 11
	s_waitcnt lgkmcnt(1)
	v_mfma_f32_32x32x16_bf16 a[0:15], v[116:119], v[124:127], a[0:15]
	v_and_b32_e32 v133, 0xffff0000, v127
	v_lshlrev_b32_e32 v102, 16, v124
	v_and_b32_e32 v103, 0xffff0000, v124
	v_lshlrev_b32_e32 v128, 16, v125
	v_and_b32_e32 v129, 0xffff0000, v125
	v_lshlrev_b32_e32 v130, 16, v126
	v_and_b32_e32 v131, 0xffff0000, v126
	v_mfma_f32_32x32x16_bf16 a[16:31], v[108:111], v[124:127], a[16:31]
	v_lshlrev_b32_e32 v132, 16, v127
	v_sub_f32_e32 v19, v19, v133
	v_sub_f32_e32 v32, v32, v102
	v_sub_f32_e32 v33, v33, v103
	v_sub_f32_e32 v34, v34, v128
	v_sub_f32_e32 v35, v35, v129
	v_sub_f32_e32 v102, v16, v130
	v_sub_f32_e32 v103, v17, v131
	v_sub_f32_e32 v128, v18, v132
	v_cvt_pk_bf16_f32 v16, v32, v33
	v_cvt_pk_bf16_f32 v17, v34, v35
	v_cvt_pk_bf16_f32 v18, v102, v103
	v_cvt_pk_bf16_f32 v19, v128, v19
	v_cvt_pk_bf16_f32 v128, v4, v5
	v_cvt_pk_bf16_f32 v129, v6, v7
	v_cvt_pk_bf16_f32 v130, v0, v1
	v_cvt_pk_bf16_f32 v131, v2, v3
	s_lshl_b32 s12, s12, 7
	v_mfma_f32_32x32x16_bf16 a[0:15], v[116:119], v[16:19], a[0:15]
	v_and_b32_e32 v35, 0xffff0000, v131
	v_lshlrev_b32_e32 v32, 16, v130
	v_and_b32_e32 v33, 0xffff0000, v130
	v_lshlrev_b32_e32 v34, 16, v131
	v_sub_f32_e32 v3, v3, v35
	s_xor_b32 s42, s42, 0x8000
	v_lshl_add_u64 v[100:101], v[100:101], 0, s[2:3]
	v_mfma_f32_32x32x16_bf16 a[16:31], v[108:111], v[16:19], a[16:31]
	ds_read_b128 v[16:19], v136 offset:6144
	ds_read_b128 v[108:111], v136 offset:7168
	s_waitcnt lgkmcnt(1)
	v_mfma_f32_32x32x16_bf16 a[0:15], v[16:19], v[124:127], a[0:15]
	ds_read_b128 v[16:19], v136 offset:2048
	ds_read_b128 v[116:119], v136 offset:3072
	s_waitcnt lgkmcnt(1)
	v_mfma_f32_32x32x16_bf16 a[16:31], v[16:19], v[124:127], a[16:31]
	v_lshlrev_b32_e32 v16, 16, v128
	v_and_b32_e32 v17, 0xffff0000, v128
	v_lshlrev_b32_e32 v18, 16, v129
	v_and_b32_e32 v19, 0xffff0000, v129
	v_sub_f32_e32 v4, v4, v16
	v_sub_f32_e32 v5, v5, v17
	v_sub_f32_e32 v6, v6, v18
	v_mfma_f32_32x32x16_bf16 a[0:15], v[120:123], v[128:131], a[0:15]
	v_sub_f32_e32 v7, v7, v19
	v_sub_f32_e32 v16, v0, v32
	v_sub_f32_e32 v17, v1, v33
	v_sub_f32_e32 v18, v2, v34
	v_cvt_pk_bf16_f32 v0, v4, v5
	v_cvt_pk_bf16_f32 v1, v6, v7
	v_cvt_pk_bf16_f32 v2, v16, v17
	v_mfma_f32_32x32x16_bf16 a[16:31], v[112:115], v[128:131], a[16:31]
	v_cvt_pk_bf16_f32 v3, v18, v3
	v_lshl_add_u64 v[4:5], v[98:99], 0, s[12:13]
	v_lshl_add_u64 v[6:7], v[4:5], 0, s[2:3]
	v_lshl_add_u64 v[16:17], v[4:5], 0, s[8:9]
	global_load_dwordx4 v[32:35], v[6:7], off
	global_load_dwordx4 v[16:19], v[16:17], off
	s_min_i32 s12, s1, 10
	v_mfma_f32_32x32x16_bf16 a[0:15], v[120:123], v[0:3], a[0:15]
	s_lshl_b32 s12, s12, 7
	v_mfma_f32_32x32x16_bf16 a[16:31], v[112:115], v[0:3], a[16:31]
	v_lshl_add_u64 v[0:1], v[4:5], 0, s[20:21]
	v_lshl_add_u64 v[2:3], v[4:5], 0, s[22:23]
	global_load_dwordx4 v[4:7], v[0:1], off
	global_load_dwordx4 v[0:3], v[2:3], off
	s_waitcnt vmcnt(20)
	s_nop 0
	v_cvt_pk_bf16_f32 v132, v40, v41
	v_mfma_f32_32x32x16_bf16 a[0:15], v[108:111], v[128:131], a[0:15]
	ds_read_b128 v[108:111], v136 offset:8192
	ds_read_b128 v[112:115], v136 offset:9216
	ds_read_b128 v[120:123], v136 offset:12288
	ds_read_b128 v[124:127], v136 offset:13312
	v_cvt_pk_bf16_f32 v133, v42, v43
	v_cvt_pk_bf16_f32 v134, v28, v29
	v_cvt_pk_bf16_f32 v135, v30, v31
	v_lshlrev_b32_e32 v102, 16, v132
	v_and_b32_e32 v103, 0xffff0000, v132
	v_sub_f32_e32 v40, v40, v102
	s_waitcnt lgkmcnt(4)
	v_mfma_f32_32x32x16_bf16 a[16:31], v[116:119], v[128:131], a[16:31]
	v_and_b32_e32 v129, 0xffff0000, v135
	v_lshlrev_b32_e32 v116, 16, v133
	v_and_b32_e32 v117, 0xffff0000, v133
	v_lshlrev_b32_e32 v118, 16, v134
	v_and_b32_e32 v119, 0xffff0000, v134
	v_lshlrev_b32_e32 v128, 16, v135
	v_sub_f32_e32 v31, v31, v129
	s_waitcnt lgkmcnt(1)
	v_mfma_f32_32x32x16_bf16 a[0:15], v[120:123], v[132:135], a[0:15]
	v_sub_f32_e32 v41, v41, v103
	v_sub_f32_e32 v42, v42, v116
	v_sub_f32_e32 v43, v43, v117
	v_sub_f32_e32 v102, v28, v118
	v_sub_f32_e32 v103, v29, v119
	v_sub_f32_e32 v116, v30, v128
	v_cvt_pk_bf16_f32 v28, v40, v41
	v_mfma_f32_32x32x16_bf16 a[16:31], v[108:111], v[132:135], a[16:31]
	v_cvt_pk_bf16_f32 v29, v42, v43
	v_cvt_pk_bf16_f32 v30, v102, v103
	v_cvt_pk_bf16_f32 v31, v116, v31
	s_nop 0
	v_mfma_f32_32x32x16_bf16 a[0:15], v[120:123], v[28:31], a[0:15]
	v_cvt_pk_bf16_f32 v120, v12, v13
	v_cvt_pk_bf16_f32 v121, v14, v15
	v_cvt_pk_bf16_f32 v122, v8, v9
	v_cvt_pk_bf16_f32 v123, v10, v11
	s_nop 0
	v_and_b32_e32 v43, 0xffff0000, v123
	v_lshlrev_b32_e32 v40, 16, v122
	v_mfma_f32_32x32x16_bf16 a[16:31], v[108:111], v[28:31], a[16:31]
	ds_read_b128 v[28:31], v136 offset:14336
	ds_read_b128 v[108:111], v136 offset:15360
	v_and_b32_e32 v41, 0xffff0000, v122
	v_lshlrev_b32_e32 v42, 16, v123
	v_sub_f32_e32 v11, v11, v43
	s_waitcnt lgkmcnt(1)
	v_mfma_f32_32x32x16_bf16 a[0:15], v[28:31], v[132:135], a[0:15]
	ds_read_b128 v[28:31], v136 offset:10240
	ds_read_b128 v[116:119], v136 offset:11264
	s_waitcnt lgkmcnt(1)
	v_mfma_f32_32x32x16_bf16 a[16:31], v[28:31], v[132:135], a[16:31]
	v_lshlrev_b32_e32 v28, 16, v120
	v_and_b32_e32 v29, 0xffff0000, v120
	v_lshlrev_b32_e32 v30, 16, v121
	v_and_b32_e32 v31, 0xffff0000, v121
	v_sub_f32_e32 v12, v12, v28
	v_sub_f32_e32 v13, v13, v29
	v_sub_f32_e32 v14, v14, v30
	v_mfma_f32_32x32x16_bf16 a[0:15], v[124:127], v[120:123], a[0:15]
	v_sub_f32_e32 v15, v15, v31
	v_sub_f32_e32 v28, v8, v40
	v_sub_f32_e32 v29, v9, v41
	v_sub_f32_e32 v30, v10, v42
	v_cvt_pk_bf16_f32 v8, v12, v13
	v_cvt_pk_bf16_f32 v9, v14, v15
	v_cvt_pk_bf16_f32 v10, v28, v29
	v_mfma_f32_32x32x16_bf16 a[16:31], v[112:115], v[120:123], a[16:31]
	v_cvt_pk_bf16_f32 v11, v30, v11
	v_lshl_add_u64 v[12:13], v[98:99], 0, s[12:13]
	v_lshl_add_u64 v[14:15], v[12:13], 0, s[24:25]
	v_lshl_add_u64 v[28:29], v[12:13], 0, s[26:27]
	global_load_dwordx4 v[40:43], v[14:15], off
	global_load_dwordx4 v[28:31], v[28:29], off
	s_min_i32 s12, s1, 9
	v_mfma_f32_32x32x16_bf16 a[0:15], v[124:127], v[8:11], a[0:15]
	s_lshl_b32 s12, s12, 7
	s_add_i32 s1, s1, 4
	s_cmp_eq_u32 s33, 4
	v_mfma_f32_32x32x16_bf16 a[16:31], v[112:115], v[8:11], a[16:31]
	v_lshl_add_u64 v[8:9], v[12:13], 0, s[28:29]
	v_lshl_add_u64 v[10:11], v[12:13], 0, s[30:31]
	global_load_dwordx4 v[12:15], v[8:9], off
	global_load_dwordx4 v[8:11], v[10:11], off
	s_waitcnt vmcnt(20)
	s_nop 0
	v_cvt_pk_bf16_f32 v132, v44, v45
	v_mfma_f32_32x32x16_bf16 a[0:15], v[108:111], v[120:123], a[0:15]
	ds_read_b128 v[108:111], v136 offset:16384
	ds_read_b128 v[112:115], v136 offset:17408
	ds_read_b128 v[124:127], v136 offset:20480
	ds_read_b128 v[128:131], v136 offset:21504
	v_cvt_pk_bf16_f32 v133, v46, v47
	v_cvt_pk_bf16_f32 v134, v36, v37
	v_cvt_pk_bf16_f32 v135, v38, v39
	v_lshlrev_b32_e32 v102, 16, v132
	v_and_b32_e32 v103, 0xffff0000, v132
	v_sub_f32_e32 v44, v44, v102
	s_waitcnt lgkmcnt(4)
	v_mfma_f32_32x32x16_bf16 a[16:31], v[116:119], v[120:123], a[16:31]
	v_and_b32_e32 v121, 0xffff0000, v135
	v_lshlrev_b32_e32 v116, 16, v133
	v_and_b32_e32 v117, 0xffff0000, v133
	v_lshlrev_b32_e32 v118, 16, v134
	v_and_b32_e32 v119, 0xffff0000, v134
	v_lshlrev_b32_e32 v120, 16, v135
	v_sub_f32_e32 v39, v39, v121
	s_waitcnt lgkmcnt(1)
	v_mfma_f32_32x32x16_bf16 a[0:15], v[124:127], v[132:135], a[0:15]
	v_sub_f32_e32 v45, v45, v103
	v_sub_f32_e32 v46, v46, v116
	v_sub_f32_e32 v47, v47, v117
	v_sub_f32_e32 v102, v36, v118
	v_sub_f32_e32 v103, v37, v119
	v_sub_f32_e32 v116, v38, v120
	v_cvt_pk_bf16_f32 v36, v44, v45
	v_mfma_f32_32x32x16_bf16 a[16:31], v[108:111], v[132:135], a[16:31]
	v_cvt_pk_bf16_f32 v37, v46, v47
	v_cvt_pk_bf16_f32 v38, v102, v103
	v_cvt_pk_bf16_f32 v39, v116, v39
	v_cvt_pk_bf16_f32 v120, v24, v25
	v_cvt_pk_bf16_f32 v121, v26, v27
	v_cvt_pk_bf16_f32 v122, v20, v21
	v_cvt_pk_bf16_f32 v123, v22, v23
	s_nop 0
	v_mfma_f32_32x32x16_bf16 a[0:15], v[124:127], v[36:39], a[0:15]
	v_and_b32_e32 v47, 0xffff0000, v123
	v_lshlrev_b32_e32 v44, 16, v122
	v_and_b32_e32 v45, 0xffff0000, v122
	v_lshlrev_b32_e32 v46, 16, v123
	v_sub_f32_e32 v23, v23, v47
	v_mfma_f32_32x32x16_bf16 a[16:31], v[108:111], v[36:39], a[16:31]
	ds_read_b128 v[36:39], v136 offset:22528
	ds_read_b128 v[108:111], v136 offset:23552
	s_waitcnt lgkmcnt(1)
	v_mfma_f32_32x32x16_bf16 a[0:15], v[36:39], v[132:135], a[0:15]
	ds_read_b128 v[36:39], v136 offset:18432
	ds_read_b128 v[116:119], v136 offset:19456
	s_waitcnt lgkmcnt(1)
	v_mfma_f32_32x32x16_bf16 a[16:31], v[36:39], v[132:135], a[16:31]
	v_lshlrev_b32_e32 v36, 16, v120
	v_and_b32_e32 v37, 0xffff0000, v120
	v_lshlrev_b32_e32 v38, 16, v121
	v_and_b32_e32 v39, 0xffff0000, v121
	v_sub_f32_e32 v24, v24, v36
	v_sub_f32_e32 v25, v25, v37
	v_sub_f32_e32 v26, v26, v38
	v_mfma_f32_32x32x16_bf16 a[0:15], v[128:131], v[120:123], a[0:15]
	v_sub_f32_e32 v27, v27, v39
	v_sub_f32_e32 v36, v20, v44
	v_sub_f32_e32 v37, v21, v45
	v_sub_f32_e32 v38, v22, v46
	v_cvt_pk_bf16_f32 v20, v24, v25
	v_cvt_pk_bf16_f32 v21, v26, v27
	v_cvt_pk_bf16_f32 v22, v36, v37
	v_mfma_f32_32x32x16_bf16 a[16:31], v[112:115], v[120:123], a[16:31]
	v_cvt_pk_bf16_f32 v23, v38, v23
	v_lshl_add_u64 v[24:25], v[98:99], 0, s[12:13]
	v_lshl_add_u64 v[26:27], v[24:25], 0, s[34:35]
	v_lshl_add_u64 v[36:37], v[24:25], 0, s[36:37]
	global_load_dwordx4 v[44:47], v[26:27], off
	global_load_dwordx4 v[36:39], v[36:37], off
	s_mov_b32 s12, s33
	v_mfma_f32_32x32x16_bf16 a[0:15], v[128:131], v[20:23], a[0:15]
	v_mfma_f32_32x32x16_bf16 a[16:31], v[112:115], v[20:23], a[16:31]
	v_lshl_add_u64 v[20:21], v[24:25], 0, s[38:39]
	v_lshl_add_u64 v[22:23], v[24:25], 0, s[40:41]
	global_load_dwordx4 v[24:27], v[20:21], off
	global_load_dwordx4 v[20:23], v[22:23], off
	s_waitcnt vmcnt(12)
	s_nop 0
	v_cvt_pk_bf16_f32 v132, v92, v93
	v_mfma_f32_32x32x16_bf16 a[0:15], v[108:111], v[120:123], a[0:15]
	ds_read_b128 v[108:111], v136 offset:24576
	ds_read_b128 v[112:115], v136 offset:25600
	ds_read_b128 v[124:127], v136 offset:28672
	ds_read_b128 v[128:131], v136 offset:29696
	v_cvt_pk_bf16_f32 v133, v94, v95
	v_cvt_pk_bf16_f32 v134, v88, v89
	v_cvt_pk_bf16_f32 v135, v90, v91
	v_lshlrev_b32_e32 v102, 16, v132
	v_and_b32_e32 v103, 0xffff0000, v132
	v_sub_f32_e32 v92, v92, v102
	s_waitcnt lgkmcnt(4)
	v_mfma_f32_32x32x16_bf16 a[16:31], v[116:119], v[120:123], a[16:31]
	v_and_b32_e32 v121, 0xffff0000, v135
	v_lshlrev_b32_e32 v116, 16, v133
	v_and_b32_e32 v117, 0xffff0000, v133
	v_lshlrev_b32_e32 v118, 16, v134
	v_and_b32_e32 v119, 0xffff0000, v134
	v_lshlrev_b32_e32 v120, 16, v135
	v_sub_f32_e32 v91, v91, v121
	s_waitcnt lgkmcnt(1)
	v_mfma_f32_32x32x16_bf16 a[0:15], v[124:127], v[132:135], a[0:15]
	v_sub_f32_e32 v93, v93, v103
	v_sub_f32_e32 v94, v94, v116
	v_sub_f32_e32 v95, v95, v117
	v_sub_f32_e32 v102, v88, v118
	v_sub_f32_e32 v103, v89, v119
	v_sub_f32_e32 v116, v90, v120
	v_cvt_pk_bf16_f32 v88, v92, v93
	v_mfma_f32_32x32x16_bf16 a[16:31], v[108:111], v[132:135], a[16:31]
	v_cvt_pk_bf16_f32 v89, v94, v95
	v_cvt_pk_bf16_f32 v90, v102, v103
	v_cvt_pk_bf16_f32 v91, v116, v91
	v_cvt_pk_bf16_f32 v116, v84, v85
	v_cvt_pk_bf16_f32 v117, v86, v87
	v_cvt_pk_bf16_f32 v118, v80, v81
	v_cvt_pk_bf16_f32 v119, v82, v83
	s_nop 0
	v_mfma_f32_32x32x16_bf16 a[0:15], v[124:127], v[88:91], a[0:15]
	v_and_b32_e32 v121, 0xffff0000, v119
	v_lshlrev_b32_e32 v102, 16, v118
	v_and_b32_e32 v103, 0xffff0000, v118
	v_lshlrev_b32_e32 v120, 16, v119
	v_sub_f32_e32 v83, v83, v121
	v_mfma_f32_32x32x16_bf16 a[16:31], v[108:111], v[88:91], a[16:31]
	ds_read_b128 v[88:91], v136 offset:30720
	ds_read_b128 v[92:95], v136 offset:31744
	s_waitcnt lgkmcnt(1)
	v_mfma_f32_32x32x16_bf16 a[0:15], v[88:91], v[132:135], a[0:15]
	ds_read_b128 v[88:91], v136 offset:26624
	ds_read_b128 v[108:111], v136 offset:27648
	s_waitcnt vmcnt(16)
	s_waitcnt lgkmcnt(1)
	v_mfma_f32_32x32x16_bf16 a[16:31], v[88:91], v[132:135], a[16:31]
	v_lshlrev_b32_e32 v88, 16, v116
	v_and_b32_e32 v89, 0xffff0000, v116
	v_lshlrev_b32_e32 v90, 16, v117
	v_and_b32_e32 v91, 0xffff0000, v117
	v_sub_f32_e32 v84, v84, v88
	v_sub_f32_e32 v85, v85, v89
	v_sub_f32_e32 v86, v86, v90
	v_mfma_f32_32x32x16_bf16 a[0:15], v[128:131], v[116:119], a[0:15]
	v_sub_f32_e32 v87, v87, v91
	v_sub_f32_e32 v88, v80, v102
	v_sub_f32_e32 v89, v81, v103
	v_sub_f32_e32 v90, v82, v120
	v_cvt_pk_bf16_f32 v80, v84, v85
	v_cvt_pk_bf16_f32 v81, v86, v87
	v_cvt_pk_bf16_f32 v82, v88, v89
	v_mfma_f32_32x32x16_bf16 a[16:31], v[112:115], v[116:119], a[16:31]
	v_cvt_pk_bf16_f32 v83, v90, v83
	s_nop 0
	v_mfma_f32_32x32x16_bf16 a[16:31], v[112:115], v[80:83], a[16:31]
	v_mfma_f32_32x32x16_bf16 a[0:15], v[128:131], v[80:83], a[0:15]
	v_add_u32_e32 v80, s42, v107
	ds_write_b128 v80, v[48:51]
	ds_write_b128 v80, v[68:71] offset:1024
	ds_write_b128 v80, v[72:75] offset:8192
	ds_write_b128 v80, v[76:79] offset:9216
	ds_write_b128 v80, v[52:55] offset:16384
	ds_write_b128 v80, v[56:59] offset:17408
	ds_write_b128 v80, v[60:63] offset:24576
	ds_write_b128 v80, v[64:67] offset:25600
	s_waitcnt lgkmcnt(0)
	s_barrier
	v_mfma_f32_32x32x16_bf16 a[16:31], v[108:111], v[116:119], a[16:31]
	v_mfma_f32_32x32x16_bf16 a[0:15], v[92:95], v[116:119], a[0:15]
	s_cbranch_scc0 .LBB5_1
	s_mov_b32 s1, 0
	s_waitcnt vmcnt(0)
	s_lshl_b64 s[0:1], s[0:1], 17
	s_add_u32 s0, s10, s0
	v_lshlrev_b32_e32 v4, 11, v105
	s_addc_u32 s1, s11, s1
	v_or_b32_e32 v5, 0x4000, v104
	v_or_b32_e32 v0, v4, v104
	v_mov_b32_e32 v1, 0
	v_lshl_add_u64 v[2:3], v[0:1], 2, s[0:1]
	v_or_b32_e32 v0, v5, v4
	global_store_dword v[2:3], a16, off sc1
	v_lshl_add_u64 v[2:3], v[0:1], 2, s[0:1]
	v_add_u32_e32 v0, v4, v104
	s_movk_i32 s2, 0x200
	global_store_dword v[2:3], a0, off sc1
	v_lshl_add_u64 v[2:3], v[0:1], 2, s[0:1]
	v_add3_u32 v0, v5, v4, s2
	v_or_b32_e32 v6, 0x400, v4
	global_store_dword v[2:3], a17, off offset:2048 sc1
	v_lshl_add_u64 v[2:3], v[0:1], 2, s[0:1]
	v_or_b32_e32 v0, v6, v104
	global_store_dword v[2:3], a1, off sc1
	v_lshl_add_u64 v[2:3], v[0:1], 2, s[0:1]
	v_or_b32_e32 v0, v5, v6
	v_or_b32_e32 v6, 0x600, v4
	global_store_dword v[2:3], a18, off sc1
	v_lshl_add_u64 v[2:3], v[0:1], 2, s[0:1]
	v_add_u32_e32 v0, v6, v104
	global_store_dword v[2:3], a2, off sc1
	v_lshl_add_u64 v[2:3], v[0:1], 2, s[0:1]
	v_add_u32_e32 v0, v5, v6
	v_or_b32_e32 v6, 0x1000, v4
	global_store_dword v[2:3], a19, off sc1
	v_lshl_add_u64 v[2:3], v[0:1], 2, s[0:1]
	v_or_b32_e32 v0, v6, v104
	global_store_dword v[2:3], a3, off sc1
	v_lshl_add_u64 v[2:3], v[0:1], 2, s[0:1]
	v_or_b32_e32 v0, v5, v6
	v_or_b32_e32 v6, 0x1200, v4
	global_store_dword v[2:3], a20, off sc1
	v_lshl_add_u64 v[2:3], v[0:1], 2, s[0:1]
	v_add_u32_e32 v0, v6, v104
	global_store_dword v[2:3], a4, off sc1
	v_lshl_add_u64 v[2:3], v[0:1], 2, s[0:1]
	v_add_u32_e32 v0, v5, v6
	v_or_b32_e32 v6, 0x1400, v4
	global_store_dword v[2:3], a21, off sc1
	v_lshl_add_u64 v[2:3], v[0:1], 2, s[0:1]
	v_or_b32_e32 v0, v6, v104
	global_store_dword v[2:3], a5, off sc1
	v_lshl_add_u64 v[2:3], v[0:1], 2, s[0:1]
	v_or_b32_e32 v0, v5, v6
	v_or_b32_e32 v6, 0x1600, v4
	global_store_dword v[2:3], a22, off sc1
	v_lshl_add_u64 v[2:3], v[0:1], 2, s[0:1]
	v_add_u32_e32 v0, v6, v104
	global_store_dword v[2:3], a6, off sc1
	v_lshl_add_u64 v[2:3], v[0:1], 2, s[0:1]
	v_add_u32_e32 v0, v5, v6
	v_or_b32_e32 v6, 0x2000, v4
	global_store_dword v[2:3], a23, off sc1
	v_lshl_add_u64 v[2:3], v[0:1], 2, s[0:1]
	v_or_b32_e32 v0, v6, v104
	global_store_dword v[2:3], a7, off sc1
	v_lshl_add_u64 v[2:3], v[0:1], 2, s[0:1]
	v_or_b32_e32 v0, v5, v6
	v_or_b32_e32 v6, 0x2200, v4
	global_store_dword v[2:3], a24, off sc1
	v_lshl_add_u64 v[2:3], v[0:1], 2, s[0:1]
	v_add_u32_e32 v0, v6, v104
	global_store_dword v[2:3], a8, off sc1
	v_lshl_add_u64 v[2:3], v[0:1], 2, s[0:1]
	v_add_u32_e32 v0, v5, v6
	v_or_b32_e32 v6, 0x2400, v4
	global_store_dword v[2:3], a25, off sc1
	v_lshl_add_u64 v[2:3], v[0:1], 2, s[0:1]
	v_or_b32_e32 v0, v6, v104
	global_store_dword v[2:3], a9, off sc1
	v_lshl_add_u64 v[2:3], v[0:1], 2, s[0:1]
	v_or_b32_e32 v0, v5, v6
	v_or_b32_e32 v6, 0x2600, v4
	global_store_dword v[2:3], a26, off sc1
	v_lshl_add_u64 v[2:3], v[0:1], 2, s[0:1]
	v_add_u32_e32 v0, v6, v104
	global_store_dword v[2:3], a10, off sc1
	v_lshl_add_u64 v[2:3], v[0:1], 2, s[0:1]
	v_add_u32_e32 v0, v5, v6
	v_or_b32_e32 v6, 0x3000, v4
	global_store_dword v[2:3], a27, off sc1
	v_lshl_add_u64 v[2:3], v[0:1], 2, s[0:1]
	v_or_b32_e32 v0, v6, v104
	global_store_dword v[2:3], a11, off sc1
	v_lshl_add_u64 v[2:3], v[0:1], 2, s[0:1]
	v_or_b32_e32 v0, v5, v6
	v_or_b32_e32 v6, 0x3200, v4
	global_store_dword v[2:3], a28, off sc1
	v_lshl_add_u64 v[2:3], v[0:1], 2, s[0:1]
	v_add_u32_e32 v0, v6, v104
	global_store_dword v[2:3], a12, off sc1
	v_lshl_add_u64 v[2:3], v[0:1], 2, s[0:1]
	v_add_u32_e32 v0, v5, v6
	v_or_b32_e32 v6, 0x3400, v4
	global_store_dword v[2:3], a29, off sc1
	v_lshl_add_u64 v[2:3], v[0:1], 2, s[0:1]
	v_or_b32_e32 v0, v6, v104
	global_store_dword v[2:3], a13, off sc1
	v_lshl_add_u64 v[2:3], v[0:1], 2, s[0:1]
	v_or_b32_e32 v0, v5, v6
	v_or_b32_e32 v4, 0x3600, v4
	global_store_dword v[2:3], a30, off sc1
	v_lshl_add_u64 v[2:3], v[0:1], 2, s[0:1]
	v_add_u32_e32 v0, v4, v104
	global_store_dword v[2:3], a14, off sc1
	v_lshl_add_u64 v[2:3], v[0:1], 2, s[0:1]
	v_add_u32_e32 v0, v5, v4
	v_lshl_add_u64 v[0:1], v[0:1], 2, s[0:1]
	global_store_dword v[2:3], a31, off sc1
	global_store_dword v[0:1], a15, off sc1
	s_endpgm
